# GU-down grid barrier made XCD-local (no L2 writeback/invalidate) when runtime placement check passes
# speedup vs baseline: 1.0194x; 1.0079x over previous
; #define LAS __attribute__((address_space(3)))
; __device__ __forceinline__ unsigned xb_add(unsigned* p, unsigned v) { return __hip_atomic_fetch_add(p, v, __ATOMIC_RELAXED, __HIP_MEMORY_SCOPE_AGENT); }
; __device__ __forceinline__ unsigned xb_xcc_id() { return (unsigned)__builtin_amdgcn_s_getreg((3 << 11) | 20) & 0xFu; }
; __device__ __forceinline__ XcdBarrier xcd_barrier_post(unsigned* bar, volatile LAS unsigned* st) {
;     XcdBarrier b; b.bar = bar; b.x = xb_xcc_id(); b.st = st;
;     if (threadIdx.x == 0) (void)xb_add(&bar[XB_XCNT(b.x)], 1u);
;     return b;
; }
.LBB0_10:
	s_or_b64 exec, exec, s[2:3]
	s_waitcnt lgkmcnt(0)
	s_barrier
	s_getreg_b32 s2, hwreg(HW_REG_XCC_ID, 0, 4)
	s_and_b32 s2, s2, 15
	v_writelane_b32 v255, s2, 7
	v_cmp_eq_u32_e64 s[4:5], 0, v228
	s_mov_b64 s[2:3], exec
	s_nop 0
	v_writelane_b32 v255, s4, 8
	s_nop 1
	v_writelane_b32 v255, s5, 9
	s_and_b64 s[4:5], s[2:3], s[4:5]
	s_mov_b64 exec, s[4:5]
	s_cbranch_execz .LBB0_13
	s_mov_b64 s[4:5], exec
	v_mbcnt_lo_u32_b32 v0, s4, 0
	v_mbcnt_hi_u32_b32 v0, s5, v0
	v_cmp_eq_u32_e32 vcc, 0, v0
	s_and_b64 s[6:7], exec, vcc
	s_mov_b64 exec, s[6:7]
	s_cbranch_execz .LBB0_13
	s_load_dwordx4 s[8:11], s[0:1], 0xd8
	v_readlane_b32 s6, v255, 7
	s_lshl_b32 s6, s6, 8
	v_mov_b32_e32 v0, 0x4000
	s_waitcnt lgkmcnt(0)
	s_add_u32 s6, s10, s6
	s_addc_u32 s7, s11, 0
	s_bcnt1_i32_b64 s4, s[4:5]
	v_mov_b32_e32 v1, s4
	global_atomic_add v0, v1, s[6:7] offset:1024
	s_and_b32 s12, s57, 7
	s_lshl_b32 s12, s12, 8
	s_add_u32 s12, s10, s12
	s_addc_u32 s13, s11, 0
	v_readlane_b32 s14, v255, 7
	s_nop 3
	s_lshl_b32 s14, 1, s14
	v_mov_b32_e32 v1, s14
	v_mov_b32_e32 v0, 0xa800
	global_atomic_or v0, v1, s[12:13]

; __device__ __forceinline__ unsigned xb_xcc_id() { return (unsigned)__builtin_amdgcn_s_getreg((3 << 11) | 20) & 0xFu; }
; __global__ void __launch_bounds__(NWAVES * 64, 2) mega_fwd(Args args) {
;     ...
;     for (int l = 0; l < LRUN; ++l) {
.LBB0_352:
	v_readlane_b32 s8, v255, 5
	v_readlane_b32 s9, v255, 6
	s_nop 3
	s_add_u32 s8, s8, 0xa800
	s_addc_u32 s9, s9, 0
	v_mov_b32_e32 v16, 0
	global_load_dword v6, v16, s[8:9] offset:0 sc1
	global_load_dword v7, v16, s[8:9] offset:256 sc1
	global_load_dword v8, v16, s[8:9] offset:512 sc1
	global_load_dword v9, v16, s[8:9] offset:768 sc1
	global_load_dword v10, v16, s[8:9] offset:1024 sc1
	global_load_dword v11, v16, s[8:9] offset:1280 sc1
	global_load_dword v12, v16, s[8:9] offset:1536 sc1
	global_load_dword v13, v16, s[8:9] offset:1792 sc1
	s_waitcnt vmcnt(0)
	v_add_u32_e32 v14, -1, v6
	v_and_b32_e32 v15, v14, v6
	v_mov_b32_e32 v17, v6
	v_add_u32_e32 v14, -1, v7
	v_and_or_b32 v15, v14, v7, v15
	v_min_u32_e32 v17, v17, v7
	v_add_u32_e32 v14, -1, v8
	v_and_or_b32 v15, v14, v8, v15
	v_min_u32_e32 v17, v17, v8
	v_add_u32_e32 v14, -1, v9
	v_and_or_b32 v15, v14, v9, v15
	v_min_u32_e32 v17, v17, v9
	v_add_u32_e32 v14, -1, v10
	v_and_or_b32 v15, v14, v10, v15
	v_min_u32_e32 v17, v17, v10
	v_add_u32_e32 v14, -1, v11
	v_and_or_b32 v15, v14, v11, v15
	v_min_u32_e32 v17, v17, v11
	v_add_u32_e32 v14, -1, v12
	v_and_or_b32 v15, v14, v12, v15
	v_min_u32_e32 v17, v17, v12
	v_add_u32_e32 v14, -1, v13
	v_and_or_b32 v15, v14, v13, v15
	v_min_u32_e32 v17, v17, v13
	s_nop 3
	v_readfirstlane_b32 s10, v15
	v_readfirstlane_b32 s11, v17
	s_nop 3
	s_cmp_eq_u32 s10, 0
	s_cselect_b32 s10, 1, 0
	s_cmp_lg_u32 s11, 0
	s_cselect_b32 s11, 1, 0
	s_and_b32 s10, s10, s11
	v_readlane_b32 s11, v255, 2
	s_nop 3
	s_cmpk_eq_u32 s11, 0x100
	s_cselect_b32 s11, 1, 0
	s_and_b32 s10, s10, s11
	s_nop 3
	v_writelane_b32 v255, s10, 40
	s_nop 3
	v_readlane_b32 s0, v255, 3
	v_readlane_b32 s2, v255, 5
	v_readlane_b32 s3, v255, 6
	s_add_u32 s0, s2, 0x7100080
	v_readlane_b32 s1, v255, 4
	v_writelane_b32 v255, s0, 12
	s_addc_u32 s0, s3, 0
	v_writelane_b32 v255, s0, 13
	s_mov_b32 s0, 1
	v_writelane_b32 v255, s0, 14
	s_add_i32 s0, 0, 0x20160
	v_writelane_b32 v255, s0, 15
	s_add_i32 s0, 0, 0x20164
	v_writelane_b32 v255, s0, 16
	s_add_i32 s0, 0, 0x14800
	v_writelane_b32 v255, s0, 17
	s_add_i32 s0, 0, 0x14900
	v_writelane_b32 v255, s0, 18
	s_mov_b32 s0, 0
	s_mov_b32 s53, 0
	s_movk_i32 s97, 0x7fff
	v_mov_b32_e32 v3, 0
	v_mov_b32_e32 v229, 0x358637bd
	s_mov_b32 s83, 0x800000
	s_mov_b32 s56, 0x45800000
	s_movk_i32 s33, 0x1a00
	s_mov_b32 s81, 0xbfb8aa3b
	s_mov_b32 s87, 0x3f2aaaab
	s_mov_b32 s82, 0x7f800000
	s_mov_b32 s86, 0x33800000
	s_movk_i32 s64, 0x1000
	s_movk_i32 s65, 0x600
	s_movk_i32 s66, 0x110
	s_movk_i32 s67, 0x800
	s_movk_i32 s68, 0x5ff
	v_mov_b32_e32 v216, 0x3ecc95a3
	s_movk_i32 s69, 0x1ff
	s_movk_i32 s70, 0x5000
	v_mov_b32_e32 v222, 0x310000
	s_movk_i32 s71, 0x2800
	s_mov_b32 s48, 0x41000000
	v_mov_b32_e32 v230, 0x7f800000
	v_mov_b32_e32 v231, 0x7fc00000
	v_mov_b32_e32 v232, 0xff800000
	v_bfrev_b32_e32 v233, 1.0
	v_mov_b32_e32 v234, 0x3f80
	v_mov_b32_e32 v235, 0x1800
	v_writelane_b32 v255, s0, 19
	s_mov_b64 s[60:61], 0x80
	s_mov_b32 s80, 0x3f317218
	s_mov_b64 s[84:85], 0x1000
	s_mov_b64 s[90:91], 0xd0000
	s_mov_b32 s96, 0x3c800000
	s_mov_b32 s49, s57
	s_branch .LBB0_356

; __device__ __forceinline__ unsigned xb_ld(unsigned* p)              { return __hip_atomic_load(p, __ATOMIC_RELAXED, __HIP_MEMORY_SCOPE_AGENT); }
; #define XB_SPIN(cond, bar) do { unsigned _sp = 0; while (cond) { __builtin_amdgcn_s_sleep(1); \
;     if ((++_sp & 255u) == 0u) { if (xb_ld(&(bar)[XB_TMO])) break; if (_sp > XB_SPIN_CAP) { atomicAdd(&(bar)[XB_TMO], 1u); break; } } } } while (0)
; __device__ __forceinline__ void xcd_barrier(const XcdBarrier& b) {
;     ...
;             XB_SPIN(xb_ld(&bar[XB_XGEN(b.x)]) == gen, bar);
;             __builtin_amdgcn_fence(__ATOMIC_ACQUIRE, XB_SCOPE);
;             asm volatile("s_waitcnt vmcnt(0)" ::: "memory");
.LBB0_3835:
	s_or_b64 exec, exec, s[8:9]
	s_waitcnt vmcnt(0) lgkmcnt(0)
	v_readlane_b32 s8, v255, 40
	s_nop 3
	s_cmp_eq_u32 s8, 1
	s_cbranch_scc1 .Lmy_nl_B10
	buffer_inv sc0 sc1
	s_branch .Lmy_nl2_B10
.Lmy_nl_B10:
	buffer_inv sc1

; __device__ __forceinline__ unsigned xb_ld(unsigned* p)              { return __hip_atomic_load(p, __ATOMIC_RELAXED, __HIP_MEMORY_SCOPE_AGENT); }
; __device__ __forceinline__ unsigned xb_add(unsigned* p, unsigned v) { return __hip_atomic_fetch_add(p, v, __ATOMIC_RELAXED, __HIP_MEMORY_SCOPE_AGENT); }
; #define XB_SPIN(cond, bar) do { unsigned _sp = 0; while (cond) { __builtin_amdgcn_s_sleep(1); \
;     if ((++_sp & 255u) == 0u) { if (xb_ld(&(bar)[XB_TMO])) break; if (_sp > XB_SPIN_CAP) { atomicAdd(&(bar)[XB_TMO], 1u); break; } } } } while (0)
; __device__ __forceinline__ void xcd_barrier(const XcdBarrier& b) {
;     ...
;         const unsigned old = xb_add(&bar[XB_XSUB(b.x)], 1u);
;         const unsigned gen = old / nloc;
;         if (old + 1u == (gen + 1u) * nloc) {
;             __builtin_amdgcn_fence(__ATOMIC_RELEASE, XB_SCOPE);
;             asm volatile("s_waitcnt vmcnt(0)" ::: "memory");
;             const unsigned og = xb_add(&bar[XB_TOP], 1u);
;             const unsigned tg = og / nx;
;             if (og + 1u == (tg + 1u) * nx) xb_add(&bar[XB_TOPGEN], 1u);
;             else XB_SPIN(xb_ld(&bar[XB_TOPGEN]) == tg, bar);
;             __builtin_amdgcn_fence(__ATOMIC_ACQUIRE, XB_SCOPE);
;             xb_add(&bar[XB_XGEN(b.x)], 1u);
;             asm volatile("s_waitcnt vmcnt(0)" ::: "memory");
.LBB0_3836:
	s_andn2_saveexec_b64 s[6:7], s[6:7]
	s_cbranch_execz .LBB0_3856
	v_readlane_b32 s8, v255, 40
	s_nop 3
	s_cmp_eq_u32 s8, 1
	s_cbranch_scc0 .Lmy_full_B10
	s_mov_b64 s[4:5], exec
	v_mbcnt_lo_u32_b32 v0, s4, 0
	v_mbcnt_hi_u32_b32 v0, s5, v0
	v_cmp_eq_u32_e32 vcc, 0, v0
	s_waitcnt vmcnt(0) lgkmcnt(0)
	buffer_inv sc1
	s_branch .Lmy_xg_B10
.Lmy_full_B10:
	s_mov_b64 s[6:7], exec
	buffer_wbl2 sc0 sc1
	s_waitcnt lgkmcnt(0)
	s_waitcnt vmcnt(0)
	v_mbcnt_lo_u32_b32 v0, s6, 0
	v_mbcnt_hi_u32_b32 v1, s7, v0
	v_cmp_eq_u32_e32 vcc, 0, v1
	s_and_saveexec_b64 s[8:9], vcc
	s_cbranch_execz .LBB0_3839
	s_bcnt1_i32_b64 s6, s[6:7]
	v_mov_b32_e32 v0, s6
	v_mov_b32_e32 v4, 0x7000
	global_atomic_add v4, v4, v0, s[4:5] offset:1024 sc0

; __device__ __forceinline__ unsigned xb_add(unsigned* p, unsigned v) { return __hip_atomic_fetch_add(p, v, __ATOMIC_RELAXED, __HIP_MEMORY_SCOPE_AGENT); }
; __device__ __forceinline__ void xcd_barrier(const XcdBarrier& b) {
;     ...
;             xb_add(&bar[XB_XGEN(b.x)], 1u);
;             asm volatile("s_waitcnt vmcnt(0)" ::: "memory");
.Lmy_xg_B10:
	s_and_saveexec_b64 s[6:7], vcc
	s_cbranch_execz .LBB0_3855
	s_add_i32 s52, s26, 0x900
	s_lshl_b64 s[8:9], s[52:53], 2
	s_add_u32 s8, s24, s8
	s_addc_u32 s9, s25, s9
	s_bcnt1_i32_b64 s4, s[4:5]
	v_mov_b32_e32 v0, s4
	global_atomic_add v3, v0, s[8:9]
